# code prefetch only at grid-barrier arrivals (waves 4..7) and phase starts (all waves), 32 KiB each; dest a0, v250 = tid*64 reserved
# speedup vs baseline: 1.0063x; 1.0063x over previous
_Z4mega5MArgs:
	v_lshlrev_b32_e32 v250, 6, v0
	s_load_dwordx4 s[28:31], s[0:1], 0xe0
	s_load_dword s33, s[0:1], 0xf0
	s_add_u32 s4, s0, 0xf0
	s_addc_u32 s5, s1, 0
	v_lshrrev_b32_e32 v1, 6, v0
	s_nop 1
	v_readfirstlane_b32 s98, v1
	v_and_b32_e32 v1, 63, v0
	v_writelane_b32 v249, s4, 0
	v_cmp_eq_u32_e32 vcc, 0, v1
	s_nop 0
	v_writelane_b32 v249, s5, 1
	s_and_saveexec_b64 s[4:5], vcc
	s_cbranch_execz .LBB0_2
	s_getreg_b32 s3, hwreg(HW_REG_HW_ID, 0, 6)
	s_lshl_b32 s3, s3, 2
	s_and_b32 s3, s3, 0xfc
	s_add_i32 s3, s3, 0
	s_add_i32 s3, s3, 0x25c00
	v_lshrrev_b32_e32 v1, 6, v0
	v_mov_b32_e32 v2, s3
	ds_write_b32 v2, v1

.LBB0_89:
	s_or_b64 exec, exec, s[6:7]
.LBB0_90:
	s_cmp_lt_i32 s28, 2
	s_cselect_b64 s[0:1], -1, 0
	s_cmp_gt_i32 s29, 2
	s_cselect_b64 s[4:5], -1, 0
	s_and_b64 s[0:1], s[0:1], s[4:5]
	s_andn2_b64 vcc, exec, s[0:1]
	s_cbranch_vccnz .LBB0_240
	s_waitcnt vmcnt(0)
	s_barrier
	s_cmp_lt_u32 s98, 4
	s_cbranch_scc1 .Lipf_a1
	s_getpc_b64 s[100:101]
	v_lshlrev_b32_e32 v251, 1, v250
	v_add_u32_e32 v251, 0xffff8000, v251
	global_load_dword a0, v251, s[100:101]
